# s16p + phase-2 conversion tail: p rows f32->bf16 in two batches of nine loads in flight (was 17-18 load+vmcnt(0)+store trips); padded
# baseline (speedup 1.0000x reference)
; DI unsigned pk2(float lo, float hi) { const f32x2 v = {lo, hi}; return __builtin_bit_cast(unsigned, __builtin_convertvector(v, bf16x2_t)); }
; template <int PART> DI void prologue_phase(const Params& P, const Frame& F) {
;     ...
;     if (PART == 1) {
;         const f32x4* src = (const f32x4*)P.in[I_P]; unsigned long long* dst = (unsigned long long*)(ws + WS_T + T_PB0);
;         for (int i = gw * 64 + F.lane; i < M * PLE / 4; i += NGW * 64) { const f32x4 pv = __builtin_nontemporal_load(src + i); dst[i] = (unsigned long long)pk2(pv[0], pv[1]) | ((unsigned long long)pk2(pv[2], pv[3]) << 32); }
;         return; }
.LBB0_219:
	global_load_dwordx4 v[206:209], v[0:1], off nt
	v_lshl_add_u64 v[0:1], v[0:1], 0, s[6:7]
	global_load_dwordx4 v[210:213], v[0:1], off nt
	v_lshl_add_u64 v[0:1], v[0:1], 0, s[6:7]
	global_load_dwordx4 v[214:217], v[0:1], off nt
	v_lshl_add_u64 v[0:1], v[0:1], 0, s[6:7]
	global_load_dwordx4 v[218:221], v[0:1], off nt
	v_lshl_add_u64 v[0:1], v[0:1], 0, s[6:7]
	global_load_dwordx4 v[222:225], v[0:1], off nt
	v_lshl_add_u64 v[0:1], v[0:1], 0, s[6:7]
	global_load_dwordx4 v[226:229], v[0:1], off nt
	v_lshl_add_u64 v[0:1], v[0:1], 0, s[6:7]
	global_load_dwordx4 v[230:233], v[0:1], off nt
	v_lshl_add_u64 v[0:1], v[0:1], 0, s[6:7]
	global_load_dwordx4 v[234:237], v[0:1], off nt
	v_lshl_add_u64 v[0:1], v[0:1], 0, s[6:7]
	global_load_dwordx4 v[238:241], v[0:1], off nt
	s_waitcnt vmcnt(8)
	v_cvt_pk_bf16_f32 v206, v206, v207
	v_cvt_pk_bf16_f32 v207, v208, v209
	global_store_dwordx2 v[2:3], v[206:207], off
	v_lshl_add_u64 v[2:3], v[2:3], 0, s[8:9]
	s_waitcnt vmcnt(8)
	v_cvt_pk_bf16_f32 v210, v210, v211
	v_cvt_pk_bf16_f32 v211, v212, v213
	global_store_dwordx2 v[2:3], v[210:211], off
	v_lshl_add_u64 v[2:3], v[2:3], 0, s[8:9]
	s_waitcnt vmcnt(8)
	v_cvt_pk_bf16_f32 v214, v214, v215
	v_cvt_pk_bf16_f32 v215, v216, v217
	global_store_dwordx2 v[2:3], v[214:215], off
	v_lshl_add_u64 v[2:3], v[2:3], 0, s[8:9]
	s_waitcnt vmcnt(8)
	v_cvt_pk_bf16_f32 v218, v218, v219
	v_cvt_pk_bf16_f32 v219, v220, v221
	global_store_dwordx2 v[2:3], v[218:219], off
	v_lshl_add_u64 v[2:3], v[2:3], 0, s[8:9]
	s_waitcnt vmcnt(8)
	v_cvt_pk_bf16_f32 v222, v222, v223
	v_cvt_pk_bf16_f32 v223, v224, v225
	global_store_dwordx2 v[2:3], v[222:223], off
	v_lshl_add_u64 v[2:3], v[2:3], 0, s[8:9]
	s_waitcnt vmcnt(8)
	v_cvt_pk_bf16_f32 v226, v226, v227
	v_cvt_pk_bf16_f32 v227, v228, v229
	global_store_dwordx2 v[2:3], v[226:227], off
	v_lshl_add_u64 v[2:3], v[2:3], 0, s[8:9]
	s_waitcnt vmcnt(8)
	v_cvt_pk_bf16_f32 v230, v230, v231
	v_cvt_pk_bf16_f32 v231, v232, v233
	global_store_dwordx2 v[2:3], v[230:231], off
	v_lshl_add_u64 v[2:3], v[2:3], 0, s[8:9]
	s_waitcnt vmcnt(8)
	v_cvt_pk_bf16_f32 v234, v234, v235
	v_cvt_pk_bf16_f32 v235, v236, v237
	global_store_dwordx2 v[2:3], v[234:235], off
	v_lshl_add_u64 v[2:3], v[2:3], 0, s[8:9]
	s_waitcnt vmcnt(8)
	v_cvt_pk_bf16_f32 v238, v238, v239
	v_cvt_pk_bf16_f32 v239, v240, v241
	global_store_dwordx2 v[2:3], v[238:239], off
	v_lshl_add_u64 v[2:3], v[2:3], 0, s[8:9]
	v_lshl_add_u64 v[0:1], v[0:1], 0, s[6:7]
	global_load_dwordx4 v[206:209], v[0:1], off nt
	v_lshl_add_u64 v[0:1], v[0:1], 0, s[6:7]
	global_load_dwordx4 v[210:213], v[0:1], off nt
	v_lshl_add_u64 v[0:1], v[0:1], 0, s[6:7]
	global_load_dwordx4 v[214:217], v[0:1], off nt
	v_lshl_add_u64 v[0:1], v[0:1], 0, s[6:7]
	global_load_dwordx4 v[218:221], v[0:1], off nt
	v_lshl_add_u64 v[0:1], v[0:1], 0, s[6:7]
	global_load_dwordx4 v[222:225], v[0:1], off nt
	v_lshl_add_u64 v[0:1], v[0:1], 0, s[6:7]
	global_load_dwordx4 v[226:229], v[0:1], off nt
	v_lshl_add_u64 v[0:1], v[0:1], 0, s[6:7]
	global_load_dwordx4 v[230:233], v[0:1], off nt
	v_lshl_add_u64 v[0:1], v[0:1], 0, s[6:7]
	global_load_dwordx4 v[234:237], v[0:1], off nt
	v_add_u32_e32 v5, 0xfac00, v4
	v_cmp_ge_i32_e32 vcc, s3, v5
	v_lshl_add_u64 v[6:7], v[0:1], 0, s[6:7]
	v_cndmask_b32_e32 v6, v0, v6, vcc
	v_cndmask_b32_e32 v7, v1, v7, vcc
	global_load_dwordx4 v[238:241], v[6:7], off nt
	s_waitcnt vmcnt(8)
	v_cvt_pk_bf16_f32 v206, v206, v207
	v_cvt_pk_bf16_f32 v207, v208, v209
	global_store_dwordx2 v[2:3], v[206:207], off
	v_lshl_add_u64 v[2:3], v[2:3], 0, s[8:9]
	s_waitcnt vmcnt(8)
	v_cvt_pk_bf16_f32 v210, v210, v211
	v_cvt_pk_bf16_f32 v211, v212, v213
	global_store_dwordx2 v[2:3], v[210:211], off
	v_lshl_add_u64 v[2:3], v[2:3], 0, s[8:9]
	s_waitcnt vmcnt(8)
	v_cvt_pk_bf16_f32 v214, v214, v215
	v_cvt_pk_bf16_f32 v215, v216, v217
	global_store_dwordx2 v[2:3], v[214:215], off
	v_lshl_add_u64 v[2:3], v[2:3], 0, s[8:9]
	s_waitcnt vmcnt(8)
	v_cvt_pk_bf16_f32 v218, v218, v219
	v_cvt_pk_bf16_f32 v219, v220, v221
	global_store_dwordx2 v[2:3], v[218:219], off
	v_lshl_add_u64 v[2:3], v[2:3], 0, s[8:9]
	s_waitcnt vmcnt(8)
	v_cvt_pk_bf16_f32 v222, v222, v223
	v_cvt_pk_bf16_f32 v223, v224, v225
	global_store_dwordx2 v[2:3], v[222:223], off
	v_lshl_add_u64 v[2:3], v[2:3], 0, s[8:9]
	s_waitcnt vmcnt(8)
	v_cvt_pk_bf16_f32 v226, v226, v227
	v_cvt_pk_bf16_f32 v227, v228, v229
	global_store_dwordx2 v[2:3], v[226:227], off
	v_lshl_add_u64 v[2:3], v[2:3], 0, s[8:9]
	s_waitcnt vmcnt(8)
	v_cvt_pk_bf16_f32 v230, v230, v231
	v_cvt_pk_bf16_f32 v231, v232, v233
	global_store_dwordx2 v[2:3], v[230:231], off
	v_lshl_add_u64 v[2:3], v[2:3], 0, s[8:9]
	s_waitcnt vmcnt(8)
	v_cvt_pk_bf16_f32 v234, v234, v235
	v_cvt_pk_bf16_f32 v235, v236, v237
	global_store_dwordx2 v[2:3], v[234:235], off
	v_lshl_add_u64 v[2:3], v[2:3], 0, s[8:9]
	s_waitcnt vmcnt(0)
	v_cvt_pk_bf16_f32 v238, v238, v239
	v_cvt_pk_bf16_f32 v239, v240, v241
	v_add_u32_e32 v5, 0xfac00, v4
	v_cmp_ge_i32_e32 vcc, s3, v5
	s_and_saveexec_b64 s[4:5], vcc
	global_store_dwordx2 v[2:3], v[238:239], off
	s_mov_b64 exec, s[4:5]
